# select pair fast path: skip per-lane list-bound compares when scalar nl_end <= 704 (slow path keeps them); unclipped counts as in baseline
# baseline (speedup 1.0000x reference)
.LBB0_1132:
	s_add_i32 s8, s33, 0x180
	s_cmp_gt_i32 s8, s10
	s_cbranch_scc1 .Lsel0_single_0
	v_and_b32_e32 v7, 0xffff, v63
	v_and_b32_e32 v13, 0xffff, v62
	v_lshrrev_b32_e32 v5, 16, v63
	v_lshrrev_b32_e32 v11, 16, v62
	v_cmp_le_u32_e64 s[18:19], s93, v7
	v_cmp_le_u32_e64 s[8:9], s93, v5
	v_cmp_le_u32_e64 s[46:47], s93, v13
	v_cmp_le_u32_e64 s[58:59], s93, v11
	v_add_u32_e32 v6, 0x80, v2
	v_add_u32_e32 v12, 0x100, v2
	v_mbcnt_lo_u32_b32 v3, s18, 0
	v_mbcnt_hi_u32_b32 v3, s19, v3
	v_mbcnt_lo_u32_b32 v9, s46, 0
	v_mbcnt_hi_u32_b32 v9, s47, v9
	s_bcnt1_i32_b64 s98, s[18:19]
	s_bcnt1_i32_b64 s99, s[8:9]
	v_mbcnt_lo_u32_b32 v3, s8, v3
	v_mbcnt_hi_u32_b32 v3, s9, v3
	s_add_i32 s98, s98, s99
	s_bcnt1_i32_b64 s99, s[46:47]
	s_bcnt1_i32_b64 s96, s[58:59]
	v_mbcnt_lo_u32_b32 v9, s58, v9
	v_mbcnt_hi_u32_b32 v9, s59, v9
	s_add_i32 s99, s99, s96
	s_add_i32 s98, s49, s98
	v_add_u32_e32 v3, s49, v3
	s_add_i32 s99, s98, s99
	v_add_u32_e32 v9, s98, v9
	v_addc_co_u32_e64 v0, s[44:45], 0, v3, s[18:19]
	v_addc_co_u32_e64 v8, s[44:45], 0, v9, s[46:47]
	s_cmpk_gt_u32 s99, 0x2c0
	s_cbranch_scc1 .Lselslow_0_0
	s_and_saveexec_b64 s[44:45], s[18:19]
	v_lshl_add_u32 v14, v3, 3, s88
	ds_write_b64 v14, v[6:7]
	s_or_b64 exec, exec, s[44:45]
	s_and_saveexec_b64 s[44:45], s[8:9]
	v_lshl_add_u32 v14, v0, 3, s88
	v_add_u32_e32 v4, 0x81, v2
	ds_write_b64 v14, v[4:5]
	s_or_b64 exec, exec, s[44:45]
	s_and_saveexec_b64 s[44:45], s[46:47]
	v_lshl_add_u32 v14, v9, 3, s88
	ds_write_b64 v14, v[12:13]
	s_or_b64 exec, exec, s[44:45]
	s_and_saveexec_b64 s[44:45], s[58:59]
	v_lshl_add_u32 v14, v8, 3, s88
	v_add_u32_e32 v10, 0x101, v2
	ds_write_b64 v14, v[10:11]
	s_or_b64 exec, exec, s[44:45]
	s_mov_b32 s49, s99
	s_branch .Lselfin_0_0
.Lselslow_0_0:
	s_movk_i32 s96, 0x2c0
	v_cmp_gt_u32_e64 s[44:45], s96, v3
	v_cmp_gt_u32_e64 s[100:101], s96, v0
	v_cmp_gt_u32_e32 vcc, s96, v9
	s_and_b64 s[18:19], s[18:19], s[44:45]
	s_and_saveexec_b64 s[44:45], s[18:19]
	v_lshl_add_u32 v14, v3, 3, s88
	ds_write_b64 v14, v[6:7]
	s_or_b64 exec, exec, s[44:45]
	s_and_b64 s[8:9], s[8:9], s[100:101]
	v_cmp_gt_u32_e64 s[100:101], s96, v8
	s_and_saveexec_b64 s[44:45], s[8:9]
	v_lshl_add_u32 v14, v0, 3, s88
	v_add_u32_e32 v4, 0x81, v2
	ds_write_b64 v14, v[4:5]
	s_or_b64 exec, exec, s[44:45]
	s_and_b64 s[46:47], s[46:47], vcc
	s_and_saveexec_b64 s[44:45], s[46:47]
	v_lshl_add_u32 v14, v9, 3, s88
	ds_write_b64 v14, v[12:13]
	s_or_b64 exec, exec, s[44:45]
	s_and_b64 s[58:59], s[58:59], s[100:101]
	s_and_saveexec_b64 s[44:45], s[58:59]
	v_lshl_add_u32 v14, v8, 3, s88
	v_add_u32_e32 v10, 0x101, v2
	ds_write_b64 v14, v[10:11]
	s_or_b64 exec, exec, s[44:45]
	s_mov_b32 s49, s99
.Lselfin_0_0:
	s_branch .Lsel0_post_0
.Lsel0_single_0:
	v_and_b32_e32 v7, 0xffff, v63
	v_add_u32_e32 v6, 0x80, v2
	v_lshrrev_b32_e32 v5, 16, v63
	v_cmp_gt_u32_e64 s[44:45], s11, v6
	v_cmp_le_u32_e32 vcc, s93, v7
	v_cmp_le_u32_e64 s[46:47], s93, v5
	s_and_b64 s[18:19], s[44:45], vcc
	v_cndmask_b32_e64 v0, 0, 1, s[18:19]
	s_and_b64 s[8:9], s[44:45], s[46:47]
	v_cmp_ne_u32_e32 vcc, 0, v0
	v_cndmask_b32_e64 v3, 0, 1, s[8:9]
	v_cmp_ne_u32_e64 s[44:45], 0, v3
	v_mbcnt_lo_u32_b32 v3, vcc_lo, 0
	v_mbcnt_hi_u32_b32 v3, vcc_hi, v3
	v_mbcnt_lo_u32_b32 v3, s44, v3
	s_min_u32 s46, s49, 0x2c0
	v_mbcnt_hi_u32_b32 v3, s45, v3
	s_lshl_b32 s47, s46, 3
	s_sub_i32 s59, 0x2c0, s46
	s_add_i32 s58, s88, s47
	v_cmp_gt_u32_e64 s[46:47], s59, v3
	s_and_b64 s[18:19], s[18:19], s[46:47]
	s_and_saveexec_b64 s[46:47], s[18:19]
	v_lshl_add_u32 v4, v3, 3, s58
	ds_write_b64 v4, v[6:7]
	s_or_b64 exec, exec, s[46:47]
	v_add_u32_e32 v0, v3, v0
	v_cmp_gt_u32_e64 s[46:47], s59, v0
	s_and_b64 s[18:19], s[8:9], s[46:47]
	s_and_saveexec_b64 s[8:9], s[18:19]
	v_lshl_add_u32 v0, v0, 3, s58
	v_add_u32_e32 v4, 0x81, v2
	ds_write_b64 v0, v[4:5]
	s_or_b64 exec, exec, s[8:9]
	s_bcnt1_i32_b64 s8, vcc
	s_bcnt1_i32_b64 s9, s[44:45]
	s_add_i32 s8, s49, s8
	s_add_i32 s49, s8, s9
	s_add_i32 s8, s33, 0x100
	s_cmp_gt_i32 s8, s10
	s_cbranch_scc1 .LBB0_1114

.LBB0_1142:
	s_add_i32 s8, s33, 0x280
	s_cmp_gt_i32 s8, s10
	s_cbranch_scc1 .Lsel0_single_2
	v_and_b32_e32 v7, 0xffff, v61
	v_and_b32_e32 v13, 0xffff, v58
	v_lshrrev_b32_e32 v5, 16, v61
	v_lshrrev_b32_e32 v11, 16, v58
	v_cmp_le_u32_e64 s[18:19], s93, v7
	v_cmp_le_u32_e64 s[8:9], s93, v5
	v_cmp_le_u32_e64 s[46:47], s93, v13
	v_cmp_le_u32_e64 s[58:59], s93, v11
	v_add_u32_e32 v6, 0x180, v2
	v_add_u32_e32 v12, 0x200, v2
	v_mbcnt_lo_u32_b32 v3, s18, 0
	v_mbcnt_hi_u32_b32 v3, s19, v3
	v_mbcnt_lo_u32_b32 v9, s46, 0
	v_mbcnt_hi_u32_b32 v9, s47, v9
	s_bcnt1_i32_b64 s98, s[18:19]
	s_bcnt1_i32_b64 s99, s[8:9]
	v_mbcnt_lo_u32_b32 v3, s8, v3
	v_mbcnt_hi_u32_b32 v3, s9, v3
	s_add_i32 s98, s98, s99
	s_bcnt1_i32_b64 s99, s[46:47]
	s_bcnt1_i32_b64 s96, s[58:59]
	v_mbcnt_lo_u32_b32 v9, s58, v9
	v_mbcnt_hi_u32_b32 v9, s59, v9
	s_add_i32 s99, s99, s96
	s_add_i32 s98, s49, s98
	v_add_u32_e32 v3, s49, v3
	s_add_i32 s99, s98, s99
	v_add_u32_e32 v9, s98, v9
	v_addc_co_u32_e64 v0, s[44:45], 0, v3, s[18:19]
	v_addc_co_u32_e64 v8, s[44:45], 0, v9, s[46:47]
	s_cmpk_gt_u32 s99, 0x2c0
	s_cbranch_scc1 .Lselslow_0_2
	s_and_saveexec_b64 s[44:45], s[18:19]
	v_lshl_add_u32 v14, v3, 3, s88
	ds_write_b64 v14, v[6:7]
	s_or_b64 exec, exec, s[44:45]
	s_and_saveexec_b64 s[44:45], s[8:9]
	v_lshl_add_u32 v14, v0, 3, s88
	v_add_u32_e32 v4, 0x181, v2
	ds_write_b64 v14, v[4:5]
	s_or_b64 exec, exec, s[44:45]
	s_and_saveexec_b64 s[44:45], s[46:47]
	v_lshl_add_u32 v14, v9, 3, s88
	ds_write_b64 v14, v[12:13]
	s_or_b64 exec, exec, s[44:45]
	s_and_saveexec_b64 s[44:45], s[58:59]
	v_lshl_add_u32 v14, v8, 3, s88
	v_add_u32_e32 v10, 0x201, v2
	ds_write_b64 v14, v[10:11]
	s_or_b64 exec, exec, s[44:45]
	s_mov_b32 s49, s99
	s_branch .Lselfin_0_2
.Lselslow_0_2:
	s_movk_i32 s96, 0x2c0
	v_cmp_gt_u32_e64 s[44:45], s96, v3
	v_cmp_gt_u32_e64 s[100:101], s96, v0
	v_cmp_gt_u32_e32 vcc, s96, v9
	s_and_b64 s[18:19], s[18:19], s[44:45]
	s_and_saveexec_b64 s[44:45], s[18:19]
	v_lshl_add_u32 v14, v3, 3, s88
	ds_write_b64 v14, v[6:7]
	s_or_b64 exec, exec, s[44:45]
	s_and_b64 s[8:9], s[8:9], s[100:101]
	v_cmp_gt_u32_e64 s[100:101], s96, v8
	s_and_saveexec_b64 s[44:45], s[8:9]
	v_lshl_add_u32 v14, v0, 3, s88
	v_add_u32_e32 v4, 0x181, v2
	ds_write_b64 v14, v[4:5]
	s_or_b64 exec, exec, s[44:45]
	s_and_b64 s[46:47], s[46:47], vcc
	s_and_saveexec_b64 s[44:45], s[46:47]
	v_lshl_add_u32 v14, v9, 3, s88
	ds_write_b64 v14, v[12:13]
	s_or_b64 exec, exec, s[44:45]
	s_and_b64 s[58:59], s[58:59], s[100:101]
	s_and_saveexec_b64 s[44:45], s[58:59]
	v_lshl_add_u32 v14, v8, 3, s88
	v_add_u32_e32 v10, 0x201, v2
	ds_write_b64 v14, v[10:11]
	s_or_b64 exec, exec, s[44:45]
	s_mov_b32 s49, s99
.Lselfin_0_2:
	s_branch .Lsel0_post_2
.Lsel0_single_2:
	v_and_b32_e32 v7, 0xffff, v61
	v_add_u32_e32 v6, 0x180, v2
	v_lshrrev_b32_e32 v5, 16, v61
	v_cmp_gt_u32_e64 s[44:45], s11, v6
	v_cmp_le_u32_e32 vcc, s93, v7
	v_cmp_le_u32_e64 s[46:47], s93, v5
	s_and_b64 s[18:19], s[44:45], vcc
	v_cndmask_b32_e64 v0, 0, 1, s[18:19]
	s_and_b64 s[8:9], s[44:45], s[46:47]
	v_cmp_ne_u32_e32 vcc, 0, v0
	v_cndmask_b32_e64 v3, 0, 1, s[8:9]
	v_cmp_ne_u32_e64 s[44:45], 0, v3
	v_mbcnt_lo_u32_b32 v3, vcc_lo, 0
	v_mbcnt_hi_u32_b32 v3, vcc_hi, v3
	v_mbcnt_lo_u32_b32 v3, s44, v3
	s_min_u32 s46, s49, 0x2c0
	v_mbcnt_hi_u32_b32 v3, s45, v3
	s_lshl_b32 s47, s46, 3
	s_sub_i32 s59, 0x2c0, s46
	s_add_i32 s58, s88, s47
	v_cmp_gt_u32_e64 s[46:47], s59, v3
	s_and_b64 s[18:19], s[18:19], s[46:47]
	s_and_saveexec_b64 s[46:47], s[18:19]
	v_lshl_add_u32 v4, v3, 3, s58
	ds_write_b64 v4, v[6:7]
	s_or_b64 exec, exec, s[46:47]
	v_add_u32_e32 v0, v3, v0
	v_cmp_gt_u32_e64 s[46:47], s59, v0
	s_and_b64 s[18:19], s[8:9], s[46:47]
	s_and_saveexec_b64 s[8:9], s[18:19]
	v_lshl_add_u32 v0, v0, 3, s58
	v_add_u32_e32 v4, 0x181, v2
	ds_write_b64 v0, v[4:5]
	s_or_b64 exec, exec, s[8:9]
	s_bcnt1_i32_b64 s8, vcc
	s_bcnt1_i32_b64 s9, s[44:45]
	s_add_i32 s8, s49, s8
	s_add_i32 s49, s8, s9
	s_add_i32 s8, s33, 0x200
	s_cmp_gt_i32 s8, s10
	s_cbranch_scc1 .LBB0_1116

.LBB0_1152:
	s_add_i32 s8, s33, 0x380
	s_cmp_gt_i32 s8, s10
	s_cbranch_scc1 .Lsel0_single_4
	v_and_b32_e32 v7, 0xffff, v59
	v_and_b32_e32 v13, 0xffff, v56
	v_lshrrev_b32_e32 v5, 16, v59
	v_lshrrev_b32_e32 v11, 16, v56
	v_cmp_le_u32_e64 s[18:19], s93, v7
	v_cmp_le_u32_e64 s[8:9], s93, v5
	v_cmp_le_u32_e64 s[46:47], s93, v13
	v_cmp_le_u32_e64 s[58:59], s93, v11
	v_add_u32_e32 v6, 0x280, v2
	v_add_u32_e32 v12, 0x300, v2
	v_mbcnt_lo_u32_b32 v3, s18, 0
	v_mbcnt_hi_u32_b32 v3, s19, v3
	v_mbcnt_lo_u32_b32 v9, s46, 0
	v_mbcnt_hi_u32_b32 v9, s47, v9
	s_bcnt1_i32_b64 s98, s[18:19]
	s_bcnt1_i32_b64 s99, s[8:9]
	v_mbcnt_lo_u32_b32 v3, s8, v3
	v_mbcnt_hi_u32_b32 v3, s9, v3
	s_add_i32 s98, s98, s99
	s_bcnt1_i32_b64 s99, s[46:47]
	s_bcnt1_i32_b64 s96, s[58:59]
	v_mbcnt_lo_u32_b32 v9, s58, v9
	v_mbcnt_hi_u32_b32 v9, s59, v9
	s_add_i32 s99, s99, s96
	s_add_i32 s98, s49, s98
	v_add_u32_e32 v3, s49, v3
	s_add_i32 s99, s98, s99
	v_add_u32_e32 v9, s98, v9
	v_addc_co_u32_e64 v0, s[44:45], 0, v3, s[18:19]
	v_addc_co_u32_e64 v8, s[44:45], 0, v9, s[46:47]
	s_cmpk_gt_u32 s99, 0x2c0
	s_cbranch_scc1 .Lselslow_0_4
	s_and_saveexec_b64 s[44:45], s[18:19]
	v_lshl_add_u32 v14, v3, 3, s88
	ds_write_b64 v14, v[6:7]
	s_or_b64 exec, exec, s[44:45]
	s_and_saveexec_b64 s[44:45], s[8:9]
	v_lshl_add_u32 v14, v0, 3, s88
	v_add_u32_e32 v4, 0x281, v2
	ds_write_b64 v14, v[4:5]
	s_or_b64 exec, exec, s[44:45]
	s_and_saveexec_b64 s[44:45], s[46:47]
	v_lshl_add_u32 v14, v9, 3, s88
	ds_write_b64 v14, v[12:13]
	s_or_b64 exec, exec, s[44:45]
	s_and_saveexec_b64 s[44:45], s[58:59]
	v_lshl_add_u32 v14, v8, 3, s88
	v_add_u32_e32 v10, 0x301, v2
	ds_write_b64 v14, v[10:11]
	s_or_b64 exec, exec, s[44:45]
	s_mov_b32 s49, s99
	s_branch .Lselfin_0_4
.Lselslow_0_4:
	s_movk_i32 s96, 0x2c0
	v_cmp_gt_u32_e64 s[44:45], s96, v3
	v_cmp_gt_u32_e64 s[100:101], s96, v0
	v_cmp_gt_u32_e32 vcc, s96, v9
	s_and_b64 s[18:19], s[18:19], s[44:45]
	s_and_saveexec_b64 s[44:45], s[18:19]
	v_lshl_add_u32 v14, v3, 3, s88
	ds_write_b64 v14, v[6:7]
	s_or_b64 exec, exec, s[44:45]
	s_and_b64 s[8:9], s[8:9], s[100:101]
	v_cmp_gt_u32_e64 s[100:101], s96, v8
	s_and_saveexec_b64 s[44:45], s[8:9]
	v_lshl_add_u32 v14, v0, 3, s88
	v_add_u32_e32 v4, 0x281, v2
	ds_write_b64 v14, v[4:5]
	s_or_b64 exec, exec, s[44:45]
	s_and_b64 s[46:47], s[46:47], vcc
	s_and_saveexec_b64 s[44:45], s[46:47]
	v_lshl_add_u32 v14, v9, 3, s88
	ds_write_b64 v14, v[12:13]
	s_or_b64 exec, exec, s[44:45]
	s_and_b64 s[58:59], s[58:59], s[100:101]
	s_and_saveexec_b64 s[44:45], s[58:59]
	v_lshl_add_u32 v14, v8, 3, s88
	v_add_u32_e32 v10, 0x301, v2
	ds_write_b64 v14, v[10:11]
	s_or_b64 exec, exec, s[44:45]
	s_mov_b32 s49, s99
.Lselfin_0_4:
	s_branch .Lsel0_post_4
.Lsel0_single_4:
	v_and_b32_e32 v7, 0xffff, v59
	v_add_u32_e32 v6, 0x280, v2
	v_lshrrev_b32_e32 v5, 16, v59
	v_cmp_gt_u32_e64 s[44:45], s11, v6
	v_cmp_le_u32_e32 vcc, s93, v7
	v_cmp_le_u32_e64 s[46:47], s93, v5
	s_and_b64 s[18:19], s[44:45], vcc
	v_cndmask_b32_e64 v0, 0, 1, s[18:19]
	s_and_b64 s[8:9], s[44:45], s[46:47]
	v_cmp_ne_u32_e32 vcc, 0, v0
	v_cndmask_b32_e64 v3, 0, 1, s[8:9]
	v_cmp_ne_u32_e64 s[44:45], 0, v3
	v_mbcnt_lo_u32_b32 v3, vcc_lo, 0
	v_mbcnt_hi_u32_b32 v3, vcc_hi, v3
	v_mbcnt_lo_u32_b32 v3, s44, v3
	s_min_u32 s46, s49, 0x2c0
	v_mbcnt_hi_u32_b32 v3, s45, v3
	s_lshl_b32 s47, s46, 3
	s_sub_i32 s59, 0x2c0, s46
	s_add_i32 s58, s88, s47
	v_cmp_gt_u32_e64 s[46:47], s59, v3
	s_and_b64 s[18:19], s[18:19], s[46:47]
	s_and_saveexec_b64 s[46:47], s[18:19]
	v_lshl_add_u32 v4, v3, 3, s58
	ds_write_b64 v4, v[6:7]
	s_or_b64 exec, exec, s[46:47]
	v_add_u32_e32 v0, v3, v0
	v_cmp_gt_u32_e64 s[46:47], s59, v0
	s_and_b64 s[18:19], s[8:9], s[46:47]
	s_and_saveexec_b64 s[8:9], s[18:19]
	v_lshl_add_u32 v0, v0, 3, s58
	v_add_u32_e32 v4, 0x281, v2
	ds_write_b64 v0, v[4:5]
	s_or_b64 exec, exec, s[8:9]
	s_bcnt1_i32_b64 s8, vcc
	s_bcnt1_i32_b64 s9, s[44:45]
	s_add_i32 s8, s49, s8
	s_add_i32 s49, s8, s9
	s_add_i32 s8, s33, 0x300
	s_cmp_gt_i32 s8, s10
	s_cbranch_scc1 .LBB0_1118

.LBB0_1162:
	s_add_i32 s8, s33, 0x480
	s_cmp_gt_i32 s8, s10
	s_cbranch_scc1 .Lsel0_single_6
	v_and_b32_e32 v7, 0xffff, v57
	v_and_b32_e32 v13, 0xffff, v54
	v_lshrrev_b32_e32 v5, 16, v57
	v_lshrrev_b32_e32 v11, 16, v54
	v_cmp_le_u32_e64 s[18:19], s93, v7
	v_cmp_le_u32_e64 s[8:9], s93, v5
	v_cmp_le_u32_e64 s[46:47], s93, v13
	v_cmp_le_u32_e64 s[58:59], s93, v11
	v_add_u32_e32 v6, 0x380, v2
	v_add_u32_e32 v12, 0x400, v2
	v_mbcnt_lo_u32_b32 v3, s18, 0
	v_mbcnt_hi_u32_b32 v3, s19, v3
	v_mbcnt_lo_u32_b32 v9, s46, 0
	v_mbcnt_hi_u32_b32 v9, s47, v9
	s_bcnt1_i32_b64 s98, s[18:19]
	s_bcnt1_i32_b64 s99, s[8:9]
	v_mbcnt_lo_u32_b32 v3, s8, v3
	v_mbcnt_hi_u32_b32 v3, s9, v3
	s_add_i32 s98, s98, s99
	s_bcnt1_i32_b64 s99, s[46:47]
	s_bcnt1_i32_b64 s96, s[58:59]
	v_mbcnt_lo_u32_b32 v9, s58, v9
	v_mbcnt_hi_u32_b32 v9, s59, v9
	s_add_i32 s99, s99, s96
	s_add_i32 s98, s49, s98
	v_add_u32_e32 v3, s49, v3
	s_add_i32 s99, s98, s99
	v_add_u32_e32 v9, s98, v9
	v_addc_co_u32_e64 v0, s[44:45], 0, v3, s[18:19]
	v_addc_co_u32_e64 v8, s[44:45], 0, v9, s[46:47]
	s_cmpk_gt_u32 s99, 0x2c0
	s_cbranch_scc1 .Lselslow_0_6
	s_and_saveexec_b64 s[44:45], s[18:19]
	v_lshl_add_u32 v14, v3, 3, s88
	ds_write_b64 v14, v[6:7]
	s_or_b64 exec, exec, s[44:45]
	s_and_saveexec_b64 s[44:45], s[8:9]
	v_lshl_add_u32 v14, v0, 3, s88
	v_add_u32_e32 v4, 0x381, v2
	ds_write_b64 v14, v[4:5]
	s_or_b64 exec, exec, s[44:45]
	s_and_saveexec_b64 s[44:45], s[46:47]
	v_lshl_add_u32 v14, v9, 3, s88
	ds_write_b64 v14, v[12:13]
	s_or_b64 exec, exec, s[44:45]
	s_and_saveexec_b64 s[44:45], s[58:59]
	v_lshl_add_u32 v14, v8, 3, s88
	v_add_u32_e32 v10, 0x401, v2
	ds_write_b64 v14, v[10:11]
	s_or_b64 exec, exec, s[44:45]
	s_mov_b32 s49, s99
	s_branch .Lselfin_0_6
.Lselslow_0_6:
	s_movk_i32 s96, 0x2c0
	v_cmp_gt_u32_e64 s[44:45], s96, v3
	v_cmp_gt_u32_e64 s[100:101], s96, v0
	v_cmp_gt_u32_e32 vcc, s96, v9
	s_and_b64 s[18:19], s[18:19], s[44:45]
	s_and_saveexec_b64 s[44:45], s[18:19]
	v_lshl_add_u32 v14, v3, 3, s88
	ds_write_b64 v14, v[6:7]
	s_or_b64 exec, exec, s[44:45]
	s_and_b64 s[8:9], s[8:9], s[100:101]
	v_cmp_gt_u32_e64 s[100:101], s96, v8
	s_and_saveexec_b64 s[44:45], s[8:9]
	v_lshl_add_u32 v14, v0, 3, s88
	v_add_u32_e32 v4, 0x381, v2
	ds_write_b64 v14, v[4:5]
	s_or_b64 exec, exec, s[44:45]
	s_and_b64 s[46:47], s[46:47], vcc
	s_and_saveexec_b64 s[44:45], s[46:47]
	v_lshl_add_u32 v14, v9, 3, s88
	ds_write_b64 v14, v[12:13]
	s_or_b64 exec, exec, s[44:45]
	s_and_b64 s[58:59], s[58:59], s[100:101]
	s_and_saveexec_b64 s[44:45], s[58:59]
	v_lshl_add_u32 v14, v8, 3, s88
	v_add_u32_e32 v10, 0x401, v2
	ds_write_b64 v14, v[10:11]
	s_or_b64 exec, exec, s[44:45]
	s_mov_b32 s49, s99
.Lselfin_0_6:
	s_branch .Lsel0_post_6
.Lsel0_single_6:
	v_and_b32_e32 v7, 0xffff, v57
	v_add_u32_e32 v6, 0x380, v2
	v_lshrrev_b32_e32 v5, 16, v57
	v_cmp_gt_u32_e64 s[44:45], s11, v6
	v_cmp_le_u32_e32 vcc, s93, v7
	v_cmp_le_u32_e64 s[46:47], s93, v5
	s_and_b64 s[18:19], s[44:45], vcc
	v_cndmask_b32_e64 v0, 0, 1, s[18:19]
	s_and_b64 s[8:9], s[44:45], s[46:47]
	v_cmp_ne_u32_e32 vcc, 0, v0
	v_cndmask_b32_e64 v3, 0, 1, s[8:9]
	v_cmp_ne_u32_e64 s[44:45], 0, v3
	v_mbcnt_lo_u32_b32 v3, vcc_lo, 0
	v_mbcnt_hi_u32_b32 v3, vcc_hi, v3
	v_mbcnt_lo_u32_b32 v3, s44, v3
	s_min_u32 s46, s49, 0x2c0
	v_mbcnt_hi_u32_b32 v3, s45, v3
	s_lshl_b32 s47, s46, 3
	s_sub_i32 s59, 0x2c0, s46
	s_add_i32 s58, s88, s47
	v_cmp_gt_u32_e64 s[46:47], s59, v3
	s_and_b64 s[18:19], s[18:19], s[46:47]
	s_and_saveexec_b64 s[46:47], s[18:19]
	v_lshl_add_u32 v4, v3, 3, s58
	ds_write_b64 v4, v[6:7]
	s_or_b64 exec, exec, s[46:47]
	v_add_u32_e32 v0, v3, v0
	v_cmp_gt_u32_e64 s[46:47], s59, v0
	s_and_b64 s[18:19], s[8:9], s[46:47]
	s_and_saveexec_b64 s[8:9], s[18:19]
	v_lshl_add_u32 v0, v0, 3, s58
	v_add_u32_e32 v4, 0x381, v2
	ds_write_b64 v0, v[4:5]
	s_or_b64 exec, exec, s[8:9]
	s_bcnt1_i32_b64 s8, vcc
	s_bcnt1_i32_b64 s9, s[44:45]
	s_add_i32 s8, s49, s8
	s_add_i32 s49, s8, s9
	s_add_i32 s8, s33, 0x400
	s_cmp_gt_i32 s8, s10
	s_cbranch_scc1 .LBB0_1120

.LBB0_1172:
	s_add_i32 s8, s33, 0x580
	s_cmp_gt_i32 s8, s10
	s_cbranch_scc1 .Lsel0_single_8
	v_and_b32_e32 v7, 0xffff, v55
	v_and_b32_e32 v13, 0xffff, v52
	v_lshrrev_b32_e32 v5, 16, v55
	v_lshrrev_b32_e32 v11, 16, v52
	v_cmp_le_u32_e64 s[18:19], s93, v7
	v_cmp_le_u32_e64 s[8:9], s93, v5
	v_cmp_le_u32_e64 s[46:47], s93, v13
	v_cmp_le_u32_e64 s[58:59], s93, v11
	v_add_u32_e32 v6, 0x480, v2
	v_add_u32_e32 v12, 0x500, v2
	v_mbcnt_lo_u32_b32 v3, s18, 0
	v_mbcnt_hi_u32_b32 v3, s19, v3
	v_mbcnt_lo_u32_b32 v9, s46, 0
	v_mbcnt_hi_u32_b32 v9, s47, v9
	s_bcnt1_i32_b64 s98, s[18:19]
	s_bcnt1_i32_b64 s99, s[8:9]
	v_mbcnt_lo_u32_b32 v3, s8, v3
	v_mbcnt_hi_u32_b32 v3, s9, v3
	s_add_i32 s98, s98, s99
	s_bcnt1_i32_b64 s99, s[46:47]
	s_bcnt1_i32_b64 s96, s[58:59]
	v_mbcnt_lo_u32_b32 v9, s58, v9
	v_mbcnt_hi_u32_b32 v9, s59, v9
	s_add_i32 s99, s99, s96
	s_add_i32 s98, s49, s98
	v_add_u32_e32 v3, s49, v3
	s_add_i32 s99, s98, s99
	v_add_u32_e32 v9, s98, v9
	v_addc_co_u32_e64 v0, s[44:45], 0, v3, s[18:19]
	v_addc_co_u32_e64 v8, s[44:45], 0, v9, s[46:47]
	s_cmpk_gt_u32 s99, 0x2c0
	s_cbranch_scc1 .Lselslow_0_8
	s_and_saveexec_b64 s[44:45], s[18:19]
	v_lshl_add_u32 v14, v3, 3, s88
	ds_write_b64 v14, v[6:7]
	s_or_b64 exec, exec, s[44:45]
	s_and_saveexec_b64 s[44:45], s[8:9]
	v_lshl_add_u32 v14, v0, 3, s88
	v_add_u32_e32 v4, 0x481, v2
	ds_write_b64 v14, v[4:5]
	s_or_b64 exec, exec, s[44:45]
	s_and_saveexec_b64 s[44:45], s[46:47]
	v_lshl_add_u32 v14, v9, 3, s88
	ds_write_b64 v14, v[12:13]
	s_or_b64 exec, exec, s[44:45]
	s_and_saveexec_b64 s[44:45], s[58:59]
	v_lshl_add_u32 v14, v8, 3, s88
	v_add_u32_e32 v10, 0x501, v2
	ds_write_b64 v14, v[10:11]
	s_or_b64 exec, exec, s[44:45]
	s_mov_b32 s49, s99
	s_branch .Lselfin_0_8
.Lselslow_0_8:
	s_movk_i32 s96, 0x2c0
	v_cmp_gt_u32_e64 s[44:45], s96, v3
	v_cmp_gt_u32_e64 s[100:101], s96, v0
	v_cmp_gt_u32_e32 vcc, s96, v9
	s_and_b64 s[18:19], s[18:19], s[44:45]
	s_and_saveexec_b64 s[44:45], s[18:19]
	v_lshl_add_u32 v14, v3, 3, s88
	ds_write_b64 v14, v[6:7]
	s_or_b64 exec, exec, s[44:45]
	s_and_b64 s[8:9], s[8:9], s[100:101]
	v_cmp_gt_u32_e64 s[100:101], s96, v8
	s_and_saveexec_b64 s[44:45], s[8:9]
	v_lshl_add_u32 v14, v0, 3, s88
	v_add_u32_e32 v4, 0x481, v2
	ds_write_b64 v14, v[4:5]
	s_or_b64 exec, exec, s[44:45]
	s_and_b64 s[46:47], s[46:47], vcc
	s_and_saveexec_b64 s[44:45], s[46:47]
	v_lshl_add_u32 v14, v9, 3, s88
	ds_write_b64 v14, v[12:13]
	s_or_b64 exec, exec, s[44:45]
	s_and_b64 s[58:59], s[58:59], s[100:101]
	s_and_saveexec_b64 s[44:45], s[58:59]
	v_lshl_add_u32 v14, v8, 3, s88
	v_add_u32_e32 v10, 0x501, v2
	ds_write_b64 v14, v[10:11]
	s_or_b64 exec, exec, s[44:45]
	s_mov_b32 s49, s99
.Lselfin_0_8:
	s_branch .Lsel0_post_8
.Lsel0_single_8:
	v_and_b32_e32 v7, 0xffff, v55
	v_add_u32_e32 v6, 0x480, v2
	v_lshrrev_b32_e32 v5, 16, v55
	v_cmp_gt_u32_e64 s[44:45], s11, v6
	v_cmp_le_u32_e32 vcc, s93, v7
	v_cmp_le_u32_e64 s[46:47], s93, v5
	s_and_b64 s[18:19], s[44:45], vcc
	v_cndmask_b32_e64 v0, 0, 1, s[18:19]
	s_and_b64 s[8:9], s[44:45], s[46:47]
	v_cmp_ne_u32_e32 vcc, 0, v0
	v_cndmask_b32_e64 v3, 0, 1, s[8:9]
	v_cmp_ne_u32_e64 s[44:45], 0, v3
	v_mbcnt_lo_u32_b32 v3, vcc_lo, 0
	v_mbcnt_hi_u32_b32 v3, vcc_hi, v3
	v_mbcnt_lo_u32_b32 v3, s44, v3
	s_min_u32 s46, s49, 0x2c0
	v_mbcnt_hi_u32_b32 v3, s45, v3
	s_lshl_b32 s47, s46, 3
	s_sub_i32 s59, 0x2c0, s46
	s_add_i32 s58, s88, s47
	v_cmp_gt_u32_e64 s[46:47], s59, v3
	s_and_b64 s[18:19], s[18:19], s[46:47]
	s_and_saveexec_b64 s[46:47], s[18:19]
	v_lshl_add_u32 v4, v3, 3, s58
	ds_write_b64 v4, v[6:7]
	s_or_b64 exec, exec, s[46:47]
	v_add_u32_e32 v0, v3, v0
	v_cmp_gt_u32_e64 s[46:47], s59, v0
	s_and_b64 s[18:19], s[8:9], s[46:47]
	s_and_saveexec_b64 s[8:9], s[18:19]
	v_lshl_add_u32 v0, v0, 3, s58
	v_add_u32_e32 v4, 0x481, v2
	ds_write_b64 v0, v[4:5]
	s_or_b64 exec, exec, s[8:9]
	s_bcnt1_i32_b64 s8, vcc
	s_bcnt1_i32_b64 s9, s[44:45]
	s_add_i32 s8, s49, s8
	s_add_i32 s49, s8, s9
	s_add_i32 s8, s33, 0x500
	s_cmp_gt_i32 s8, s10
	s_cbranch_scc1 .LBB0_1122

.LBB0_1182:
	s_add_i32 s8, s33, 0x680
	s_cmp_gt_i32 s8, s10
	s_cbranch_scc1 .Lsel0_single_10
	v_and_b32_e32 v7, 0xffff, v53
	v_and_b32_e32 v13, 0xffff, v34
	v_lshrrev_b32_e32 v5, 16, v53
	v_lshrrev_b32_e32 v11, 16, v34
	v_cmp_le_u32_e64 s[18:19], s93, v7
	v_cmp_le_u32_e64 s[8:9], s93, v5
	v_cmp_le_u32_e64 s[46:47], s93, v13
	v_cmp_le_u32_e64 s[58:59], s93, v11
	v_add_u32_e32 v6, 0x580, v2
	v_add_u32_e32 v12, 0x600, v2
	v_mbcnt_lo_u32_b32 v3, s18, 0
	v_mbcnt_hi_u32_b32 v3, s19, v3
	v_mbcnt_lo_u32_b32 v9, s46, 0
	v_mbcnt_hi_u32_b32 v9, s47, v9
	s_bcnt1_i32_b64 s98, s[18:19]
	s_bcnt1_i32_b64 s99, s[8:9]
	v_mbcnt_lo_u32_b32 v3, s8, v3
	v_mbcnt_hi_u32_b32 v3, s9, v3
	s_add_i32 s98, s98, s99
	s_bcnt1_i32_b64 s99, s[46:47]
	s_bcnt1_i32_b64 s96, s[58:59]
	v_mbcnt_lo_u32_b32 v9, s58, v9
	v_mbcnt_hi_u32_b32 v9, s59, v9
	s_add_i32 s99, s99, s96
	s_add_i32 s98, s49, s98
	v_add_u32_e32 v3, s49, v3
	s_add_i32 s99, s98, s99
	v_add_u32_e32 v9, s98, v9
	v_addc_co_u32_e64 v0, s[44:45], 0, v3, s[18:19]
	v_addc_co_u32_e64 v8, s[44:45], 0, v9, s[46:47]
	s_cmpk_gt_u32 s99, 0x2c0
	s_cbranch_scc1 .Lselslow_0_10
	s_and_saveexec_b64 s[44:45], s[18:19]
	v_lshl_add_u32 v14, v3, 3, s88
	ds_write_b64 v14, v[6:7]
	s_or_b64 exec, exec, s[44:45]
	s_and_saveexec_b64 s[44:45], s[8:9]
	v_lshl_add_u32 v14, v0, 3, s88
	v_add_u32_e32 v4, 0x581, v2
	ds_write_b64 v14, v[4:5]
	s_or_b64 exec, exec, s[44:45]
	s_and_saveexec_b64 s[44:45], s[46:47]
	v_lshl_add_u32 v14, v9, 3, s88
	ds_write_b64 v14, v[12:13]
	s_or_b64 exec, exec, s[44:45]
	s_and_saveexec_b64 s[44:45], s[58:59]
	v_lshl_add_u32 v14, v8, 3, s88
	v_add_u32_e32 v10, 0x601, v2
	ds_write_b64 v14, v[10:11]
	s_or_b64 exec, exec, s[44:45]
	s_mov_b32 s49, s99
	s_branch .Lselfin_0_10
.Lselslow_0_10:
	s_movk_i32 s96, 0x2c0
	v_cmp_gt_u32_e64 s[44:45], s96, v3
	v_cmp_gt_u32_e64 s[100:101], s96, v0
	v_cmp_gt_u32_e32 vcc, s96, v9
	s_and_b64 s[18:19], s[18:19], s[44:45]
	s_and_saveexec_b64 s[44:45], s[18:19]
	v_lshl_add_u32 v14, v3, 3, s88
	ds_write_b64 v14, v[6:7]
	s_or_b64 exec, exec, s[44:45]
	s_and_b64 s[8:9], s[8:9], s[100:101]
	v_cmp_gt_u32_e64 s[100:101], s96, v8
	s_and_saveexec_b64 s[44:45], s[8:9]
	v_lshl_add_u32 v14, v0, 3, s88
	v_add_u32_e32 v4, 0x581, v2
	ds_write_b64 v14, v[4:5]
	s_or_b64 exec, exec, s[44:45]
	s_and_b64 s[46:47], s[46:47], vcc
	s_and_saveexec_b64 s[44:45], s[46:47]
	v_lshl_add_u32 v14, v9, 3, s88
	ds_write_b64 v14, v[12:13]
	s_or_b64 exec, exec, s[44:45]
	s_and_b64 s[58:59], s[58:59], s[100:101]
	s_and_saveexec_b64 s[44:45], s[58:59]
	v_lshl_add_u32 v14, v8, 3, s88
	v_add_u32_e32 v10, 0x601, v2
	ds_write_b64 v14, v[10:11]
	s_or_b64 exec, exec, s[44:45]
	s_mov_b32 s49, s99
.Lselfin_0_10:
	s_branch .Lsel0_post_10
.Lsel0_single_10:
	v_and_b32_e32 v7, 0xffff, v53
	v_add_u32_e32 v6, 0x580, v2
	v_lshrrev_b32_e32 v5, 16, v53
	v_cmp_gt_u32_e64 s[44:45], s11, v6
	v_cmp_le_u32_e32 vcc, s93, v7
	v_cmp_le_u32_e64 s[46:47], s93, v5
	s_and_b64 s[18:19], s[44:45], vcc
	v_cndmask_b32_e64 v0, 0, 1, s[18:19]
	s_and_b64 s[8:9], s[44:45], s[46:47]
	v_cmp_ne_u32_e32 vcc, 0, v0
	v_cndmask_b32_e64 v3, 0, 1, s[8:9]
	v_cmp_ne_u32_e64 s[44:45], 0, v3
	v_mbcnt_lo_u32_b32 v3, vcc_lo, 0
	v_mbcnt_hi_u32_b32 v3, vcc_hi, v3
	v_mbcnt_lo_u32_b32 v3, s44, v3
	s_min_u32 s46, s49, 0x2c0
	v_mbcnt_hi_u32_b32 v3, s45, v3
	s_lshl_b32 s47, s46, 3
	s_sub_i32 s59, 0x2c0, s46
	s_add_i32 s58, s88, s47
	v_cmp_gt_u32_e64 s[46:47], s59, v3
	s_and_b64 s[18:19], s[18:19], s[46:47]
	s_and_saveexec_b64 s[46:47], s[18:19]
	v_lshl_add_u32 v4, v3, 3, s58
	ds_write_b64 v4, v[6:7]
	s_or_b64 exec, exec, s[46:47]
	v_add_u32_e32 v0, v3, v0
	v_cmp_gt_u32_e64 s[46:47], s59, v0
	s_and_b64 s[18:19], s[8:9], s[46:47]
	s_and_saveexec_b64 s[8:9], s[18:19]
	v_lshl_add_u32 v0, v0, 3, s58
	v_add_u32_e32 v4, 0x581, v2
	ds_write_b64 v0, v[4:5]
	s_or_b64 exec, exec, s[8:9]
	s_bcnt1_i32_b64 s8, vcc
	s_bcnt1_i32_b64 s9, s[44:45]
	s_add_i32 s8, s49, s8
	s_add_i32 s49, s8, s9
	s_add_i32 s8, s33, 0x600
	s_cmp_gt_i32 s8, s10
	s_cbranch_scc1 .LBB0_1124

.LBB0_1192:
	s_add_i32 s8, s33, 0x780
	s_cmp_gt_i32 s8, s10
	s_cbranch_scc1 .Lsel0_single_12
	v_and_b32_e32 v7, 0xffff, v35
	v_and_b32_e32 v13, 0xffff, v32
	v_lshrrev_b32_e32 v5, 16, v35
	v_lshrrev_b32_e32 v11, 16, v32
	v_cmp_le_u32_e64 s[18:19], s93, v7
	v_cmp_le_u32_e64 s[8:9], s93, v5
	v_cmp_le_u32_e64 s[46:47], s93, v13
	v_cmp_le_u32_e64 s[58:59], s93, v11
	v_add_u32_e32 v6, 0x680, v2
	v_add_u32_e32 v12, 0x700, v2
	v_mbcnt_lo_u32_b32 v3, s18, 0
	v_mbcnt_hi_u32_b32 v3, s19, v3
	v_mbcnt_lo_u32_b32 v9, s46, 0
	v_mbcnt_hi_u32_b32 v9, s47, v9
	s_bcnt1_i32_b64 s98, s[18:19]
	s_bcnt1_i32_b64 s99, s[8:9]
	v_mbcnt_lo_u32_b32 v3, s8, v3
	v_mbcnt_hi_u32_b32 v3, s9, v3
	s_add_i32 s98, s98, s99
	s_bcnt1_i32_b64 s99, s[46:47]
	s_bcnt1_i32_b64 s96, s[58:59]
	v_mbcnt_lo_u32_b32 v9, s58, v9
	v_mbcnt_hi_u32_b32 v9, s59, v9
	s_add_i32 s99, s99, s96
	s_add_i32 s98, s49, s98
	v_add_u32_e32 v3, s49, v3
	s_add_i32 s99, s98, s99
	v_add_u32_e32 v9, s98, v9
	v_addc_co_u32_e64 v0, s[44:45], 0, v3, s[18:19]
	v_addc_co_u32_e64 v8, s[44:45], 0, v9, s[46:47]
	s_cmpk_gt_u32 s99, 0x2c0
	s_cbranch_scc1 .Lselslow_0_12
	s_and_saveexec_b64 s[44:45], s[18:19]
	v_lshl_add_u32 v14, v3, 3, s88
	ds_write_b64 v14, v[6:7]
	s_or_b64 exec, exec, s[44:45]
	s_and_saveexec_b64 s[44:45], s[8:9]
	v_lshl_add_u32 v14, v0, 3, s88
	v_add_u32_e32 v4, 0x681, v2
	ds_write_b64 v14, v[4:5]
	s_or_b64 exec, exec, s[44:45]
	s_and_saveexec_b64 s[44:45], s[46:47]
	v_lshl_add_u32 v14, v9, 3, s88
	ds_write_b64 v14, v[12:13]
	s_or_b64 exec, exec, s[44:45]
	s_and_saveexec_b64 s[44:45], s[58:59]
	v_lshl_add_u32 v14, v8, 3, s88
	v_add_u32_e32 v10, 0x701, v2
	ds_write_b64 v14, v[10:11]
	s_or_b64 exec, exec, s[44:45]
	s_mov_b32 s49, s99
	s_branch .Lselfin_0_12
.Lselslow_0_12:
	s_movk_i32 s96, 0x2c0
	v_cmp_gt_u32_e64 s[44:45], s96, v3
	v_cmp_gt_u32_e64 s[100:101], s96, v0
	v_cmp_gt_u32_e32 vcc, s96, v9
	s_and_b64 s[18:19], s[18:19], s[44:45]
	s_and_saveexec_b64 s[44:45], s[18:19]
	v_lshl_add_u32 v14, v3, 3, s88
	ds_write_b64 v14, v[6:7]
	s_or_b64 exec, exec, s[44:45]
	s_and_b64 s[8:9], s[8:9], s[100:101]
	v_cmp_gt_u32_e64 s[100:101], s96, v8
	s_and_saveexec_b64 s[44:45], s[8:9]
	v_lshl_add_u32 v14, v0, 3, s88
	v_add_u32_e32 v4, 0x681, v2
	ds_write_b64 v14, v[4:5]
	s_or_b64 exec, exec, s[44:45]
	s_and_b64 s[46:47], s[46:47], vcc
	s_and_saveexec_b64 s[44:45], s[46:47]
	v_lshl_add_u32 v14, v9, 3, s88
	ds_write_b64 v14, v[12:13]
	s_or_b64 exec, exec, s[44:45]
	s_and_b64 s[58:59], s[58:59], s[100:101]
	s_and_saveexec_b64 s[44:45], s[58:59]
	v_lshl_add_u32 v14, v8, 3, s88
	v_add_u32_e32 v10, 0x701, v2
	ds_write_b64 v14, v[10:11]
	s_or_b64 exec, exec, s[44:45]
	s_mov_b32 s49, s99
.Lselfin_0_12:
	s_branch .Lsel0_post_12
.Lsel0_single_12:
	v_and_b32_e32 v7, 0xffff, v35
	v_add_u32_e32 v6, 0x680, v2
	v_lshrrev_b32_e32 v5, 16, v35
	v_cmp_gt_u32_e64 s[44:45], s11, v6
	v_cmp_le_u32_e32 vcc, s93, v7
	v_cmp_le_u32_e64 s[46:47], s93, v5
	s_and_b64 s[18:19], s[44:45], vcc
	v_cndmask_b32_e64 v0, 0, 1, s[18:19]
	s_and_b64 s[8:9], s[44:45], s[46:47]
	v_cmp_ne_u32_e32 vcc, 0, v0
	v_cndmask_b32_e64 v3, 0, 1, s[8:9]
	v_cmp_ne_u32_e64 s[44:45], 0, v3
	v_mbcnt_lo_u32_b32 v3, vcc_lo, 0
	v_mbcnt_hi_u32_b32 v3, vcc_hi, v3
	v_mbcnt_lo_u32_b32 v3, s44, v3
	s_min_u32 s46, s49, 0x2c0
	v_mbcnt_hi_u32_b32 v3, s45, v3
	s_lshl_b32 s47, s46, 3
	s_sub_i32 s59, 0x2c0, s46
	s_add_i32 s58, s88, s47
	v_cmp_gt_u32_e64 s[46:47], s59, v3
	s_and_b64 s[18:19], s[18:19], s[46:47]
	s_and_saveexec_b64 s[46:47], s[18:19]
	v_lshl_add_u32 v4, v3, 3, s58
	ds_write_b64 v4, v[6:7]
	s_or_b64 exec, exec, s[46:47]
	v_add_u32_e32 v0, v3, v0
	v_cmp_gt_u32_e64 s[46:47], s59, v0
	s_and_b64 s[18:19], s[8:9], s[46:47]
	s_and_saveexec_b64 s[8:9], s[18:19]
	v_lshl_add_u32 v0, v0, 3, s58
	v_add_u32_e32 v4, 0x681, v2
	ds_write_b64 v0, v[4:5]
	s_or_b64 exec, exec, s[8:9]
	s_bcnt1_i32_b64 s8, vcc
	s_bcnt1_i32_b64 s9, s[44:45]
	s_add_i32 s8, s49, s8
	s_add_i32 s49, s8, s9
	s_add_i32 s8, s33, 0x700
	s_cmp_gt_i32 s8, s10
	s_cbranch_scc1 .LBB0_1126

.LBB0_1235:
	s_add_i32 s8, s30, 0x180
	s_cmp_gt_i32 s8, s10
	s_cbranch_scc1 .Lsel1_single_0
	v_and_b32_e32 v7, 0xffff, v17
	v_and_b32_e32 v13, 0xffff, v18
	v_lshrrev_b32_e32 v5, 16, v17
	v_lshrrev_b32_e32 v11, 16, v18
	v_cmp_le_u32_e64 s[18:19], s29, v7
	v_cmp_le_u32_e64 s[8:9], s29, v5
	v_cmp_le_u32_e64 s[46:47], s29, v13
	v_cmp_le_u32_e64 s[58:59], s29, v11
	v_add_u32_e32 v6, 0x80, v2
	v_add_u32_e32 v12, 0x100, v2
	v_mbcnt_lo_u32_b32 v3, s18, 0
	v_mbcnt_hi_u32_b32 v3, s19, v3
	v_mbcnt_lo_u32_b32 v9, s46, 0
	v_mbcnt_hi_u32_b32 v9, s47, v9
	s_bcnt1_i32_b64 s98, s[18:19]
	s_bcnt1_i32_b64 s99, s[8:9]
	v_mbcnt_lo_u32_b32 v3, s8, v3
	v_mbcnt_hi_u32_b32 v3, s9, v3
	s_add_i32 s98, s98, s99
	s_bcnt1_i32_b64 s99, s[46:47]
	s_bcnt1_i32_b64 s96, s[58:59]
	v_mbcnt_lo_u32_b32 v9, s58, v9
	v_mbcnt_hi_u32_b32 v9, s59, v9
	s_add_i32 s99, s99, s96
	s_add_i32 s98, s28, s98
	v_add_u32_e32 v3, s28, v3
	s_add_i32 s99, s98, s99
	v_add_u32_e32 v9, s98, v9
	v_addc_co_u32_e64 v0, s[44:45], 0, v3, s[18:19]
	v_addc_co_u32_e64 v8, s[44:45], 0, v9, s[46:47]
	s_cmpk_gt_u32 s99, 0x2c0
	s_cbranch_scc1 .Lselslow_1_0
	s_and_saveexec_b64 s[44:45], s[18:19]
	v_lshl_add_u32 v14, v3, 3, s88
	ds_write_b64 v14, v[6:7]
	s_or_b64 exec, exec, s[44:45]
	s_and_saveexec_b64 s[44:45], s[8:9]
	v_lshl_add_u32 v14, v0, 3, s88
	v_add_u32_e32 v4, 0x81, v2
	ds_write_b64 v14, v[4:5]
	s_or_b64 exec, exec, s[44:45]
	s_and_saveexec_b64 s[44:45], s[46:47]
	v_lshl_add_u32 v14, v9, 3, s88
	ds_write_b64 v14, v[12:13]
	s_or_b64 exec, exec, s[44:45]
	s_and_saveexec_b64 s[44:45], s[58:59]
	v_lshl_add_u32 v14, v8, 3, s88
	v_add_u32_e32 v10, 0x101, v2
	ds_write_b64 v14, v[10:11]
	s_or_b64 exec, exec, s[44:45]
	s_mov_b32 s28, s99
	s_branch .Lselfin_1_0
.Lselslow_1_0:
	s_movk_i32 s96, 0x2c0
	v_cmp_gt_u32_e64 s[44:45], s96, v3
	v_cmp_gt_u32_e64 s[100:101], s96, v0
	v_cmp_gt_u32_e32 vcc, s96, v9
	s_and_b64 s[18:19], s[18:19], s[44:45]
	s_and_saveexec_b64 s[44:45], s[18:19]
	v_lshl_add_u32 v14, v3, 3, s88
	ds_write_b64 v14, v[6:7]
	s_or_b64 exec, exec, s[44:45]
	s_and_b64 s[8:9], s[8:9], s[100:101]
	v_cmp_gt_u32_e64 s[100:101], s96, v8
	s_and_saveexec_b64 s[44:45], s[8:9]
	v_lshl_add_u32 v14, v0, 3, s88
	v_add_u32_e32 v4, 0x81, v2
	ds_write_b64 v14, v[4:5]
	s_or_b64 exec, exec, s[44:45]
	s_and_b64 s[46:47], s[46:47], vcc
	s_and_saveexec_b64 s[44:45], s[46:47]
	v_lshl_add_u32 v14, v9, 3, s88
	ds_write_b64 v14, v[12:13]
	s_or_b64 exec, exec, s[44:45]
	s_and_b64 s[58:59], s[58:59], s[100:101]
	s_and_saveexec_b64 s[44:45], s[58:59]
	v_lshl_add_u32 v14, v8, 3, s88
	v_add_u32_e32 v10, 0x101, v2
	ds_write_b64 v14, v[10:11]
	s_or_b64 exec, exec, s[44:45]
	s_mov_b32 s28, s99
.Lselfin_1_0:
	s_branch .Lsel1_post_0
.Lsel1_single_0:
	v_and_b32_e32 v7, 0xffff, v17
	v_add_u32_e32 v6, 0x80, v2
	v_lshrrev_b32_e32 v5, 16, v17
	v_cmp_gt_u32_e64 s[44:45], s11, v6
	v_cmp_le_u32_e32 vcc, s29, v7
	v_cmp_le_u32_e64 s[46:47], s29, v5
	s_and_b64 s[18:19], s[44:45], vcc
	v_cndmask_b32_e64 v0, 0, 1, s[18:19]
	s_and_b64 s[8:9], s[44:45], s[46:47]
	v_cmp_ne_u32_e32 vcc, 0, v0
	v_cndmask_b32_e64 v3, 0, 1, s[8:9]
	v_cmp_ne_u32_e64 s[44:45], 0, v3
	v_mbcnt_lo_u32_b32 v3, vcc_lo, 0
	v_mbcnt_hi_u32_b32 v3, vcc_hi, v3
	v_mbcnt_lo_u32_b32 v3, s44, v3
	s_min_u32 s26, s28, 0x2c0
	v_mbcnt_hi_u32_b32 v3, s45, v3
	s_sub_i32 s33, 0x2c0, s26
	s_lshl_b32 s27, s26, 3
	v_cmp_gt_u32_e64 s[46:47], s33, v3
	s_add_i32 s31, s88, s27
	s_and_b64 s[18:19], s[18:19], s[46:47]
	s_and_saveexec_b64 s[26:27], s[18:19]
	v_lshl_add_u32 v4, v3, 3, s31
	ds_write_b64 v4, v[6:7]
	s_or_b64 exec, exec, s[26:27]
	v_add_u32_e32 v0, v3, v0
	v_cmp_gt_u32_e64 s[46:47], s33, v0
	s_and_b64 s[18:19], s[8:9], s[46:47]
	s_and_saveexec_b64 s[8:9], s[18:19]
	v_lshl_add_u32 v0, v0, 3, s31
	v_add_u32_e32 v4, 0x81, v2
	ds_write_b64 v0, v[4:5]
	s_or_b64 exec, exec, s[8:9]
	s_bcnt1_i32_b64 s8, vcc
	s_bcnt1_i32_b64 s9, s[44:45]
	s_add_i32 s8, s28, s8
	s_add_i32 s28, s8, s9
	s_add_i32 s8, s30, 0x100
	s_cmp_gt_i32 s8, s10
	s_cbranch_scc1 .LBB0_1217

.LBB0_1245:
	s_add_i32 s8, s30, 0x280
	s_cmp_gt_i32 s8, s10
	s_cbranch_scc1 .Lsel1_single_2
	v_and_b32_e32 v7, 0xffff, v19
	v_and_b32_e32 v13, 0xffff, v20
	v_lshrrev_b32_e32 v5, 16, v19
	v_lshrrev_b32_e32 v11, 16, v20
	v_cmp_le_u32_e64 s[18:19], s29, v7
	v_cmp_le_u32_e64 s[8:9], s29, v5
	v_cmp_le_u32_e64 s[46:47], s29, v13
	v_cmp_le_u32_e64 s[58:59], s29, v11
	v_add_u32_e32 v6, 0x180, v2
	v_add_u32_e32 v12, 0x200, v2
	v_mbcnt_lo_u32_b32 v3, s18, 0
	v_mbcnt_hi_u32_b32 v3, s19, v3
	v_mbcnt_lo_u32_b32 v9, s46, 0
	v_mbcnt_hi_u32_b32 v9, s47, v9
	s_bcnt1_i32_b64 s98, s[18:19]
	s_bcnt1_i32_b64 s99, s[8:9]
	v_mbcnt_lo_u32_b32 v3, s8, v3
	v_mbcnt_hi_u32_b32 v3, s9, v3
	s_add_i32 s98, s98, s99
	s_bcnt1_i32_b64 s99, s[46:47]
	s_bcnt1_i32_b64 s96, s[58:59]
	v_mbcnt_lo_u32_b32 v9, s58, v9
	v_mbcnt_hi_u32_b32 v9, s59, v9
	s_add_i32 s99, s99, s96
	s_add_i32 s98, s28, s98
	v_add_u32_e32 v3, s28, v3
	s_add_i32 s99, s98, s99
	v_add_u32_e32 v9, s98, v9
	v_addc_co_u32_e64 v0, s[44:45], 0, v3, s[18:19]
	v_addc_co_u32_e64 v8, s[44:45], 0, v9, s[46:47]
	s_cmpk_gt_u32 s99, 0x2c0
	s_cbranch_scc1 .Lselslow_1_2
	s_and_saveexec_b64 s[44:45], s[18:19]
	v_lshl_add_u32 v14, v3, 3, s88
	ds_write_b64 v14, v[6:7]
	s_or_b64 exec, exec, s[44:45]
	s_and_saveexec_b64 s[44:45], s[8:9]
	v_lshl_add_u32 v14, v0, 3, s88
	v_add_u32_e32 v4, 0x181, v2
	ds_write_b64 v14, v[4:5]
	s_or_b64 exec, exec, s[44:45]
	s_and_saveexec_b64 s[44:45], s[46:47]
	v_lshl_add_u32 v14, v9, 3, s88
	ds_write_b64 v14, v[12:13]
	s_or_b64 exec, exec, s[44:45]
	s_and_saveexec_b64 s[44:45], s[58:59]
	v_lshl_add_u32 v14, v8, 3, s88
	v_add_u32_e32 v10, 0x201, v2
	ds_write_b64 v14, v[10:11]
	s_or_b64 exec, exec, s[44:45]
	s_mov_b32 s28, s99
	s_branch .Lselfin_1_2
.Lselslow_1_2:
	s_movk_i32 s96, 0x2c0
	v_cmp_gt_u32_e64 s[44:45], s96, v3
	v_cmp_gt_u32_e64 s[100:101], s96, v0
	v_cmp_gt_u32_e32 vcc, s96, v9
	s_and_b64 s[18:19], s[18:19], s[44:45]
	s_and_saveexec_b64 s[44:45], s[18:19]
	v_lshl_add_u32 v14, v3, 3, s88
	ds_write_b64 v14, v[6:7]
	s_or_b64 exec, exec, s[44:45]
	s_and_b64 s[8:9], s[8:9], s[100:101]
	v_cmp_gt_u32_e64 s[100:101], s96, v8
	s_and_saveexec_b64 s[44:45], s[8:9]
	v_lshl_add_u32 v14, v0, 3, s88
	v_add_u32_e32 v4, 0x181, v2
	ds_write_b64 v14, v[4:5]
	s_or_b64 exec, exec, s[44:45]
	s_and_b64 s[46:47], s[46:47], vcc
	s_and_saveexec_b64 s[44:45], s[46:47]
	v_lshl_add_u32 v14, v9, 3, s88
	ds_write_b64 v14, v[12:13]
	s_or_b64 exec, exec, s[44:45]
	s_and_b64 s[58:59], s[58:59], s[100:101]
	s_and_saveexec_b64 s[44:45], s[58:59]
	v_lshl_add_u32 v14, v8, 3, s88
	v_add_u32_e32 v10, 0x201, v2
	ds_write_b64 v14, v[10:11]
	s_or_b64 exec, exec, s[44:45]
	s_mov_b32 s28, s99
.Lselfin_1_2:
	s_branch .Lsel1_post_2
.Lsel1_single_2:
	v_and_b32_e32 v7, 0xffff, v19
	v_add_u32_e32 v6, 0x180, v2
	v_lshrrev_b32_e32 v5, 16, v19
	v_cmp_gt_u32_e64 s[44:45], s11, v6
	v_cmp_le_u32_e32 vcc, s29, v7
	v_cmp_le_u32_e64 s[46:47], s29, v5
	s_and_b64 s[18:19], s[44:45], vcc
	v_cndmask_b32_e64 v0, 0, 1, s[18:19]
	s_and_b64 s[8:9], s[44:45], s[46:47]
	v_cmp_ne_u32_e32 vcc, 0, v0
	v_cndmask_b32_e64 v3, 0, 1, s[8:9]
	v_cmp_ne_u32_e64 s[44:45], 0, v3
	v_mbcnt_lo_u32_b32 v3, vcc_lo, 0
	v_mbcnt_hi_u32_b32 v3, vcc_hi, v3
	v_mbcnt_lo_u32_b32 v3, s44, v3
	s_min_u32 s26, s28, 0x2c0
	v_mbcnt_hi_u32_b32 v3, s45, v3
	s_sub_i32 s33, 0x2c0, s26
	s_lshl_b32 s27, s26, 3
	v_cmp_gt_u32_e64 s[46:47], s33, v3
	s_add_i32 s31, s88, s27
	s_and_b64 s[18:19], s[18:19], s[46:47]
	s_and_saveexec_b64 s[26:27], s[18:19]
	v_lshl_add_u32 v4, v3, 3, s31
	ds_write_b64 v4, v[6:7]
	s_or_b64 exec, exec, s[26:27]
	v_add_u32_e32 v0, v3, v0
	v_cmp_gt_u32_e64 s[46:47], s33, v0
	s_and_b64 s[18:19], s[8:9], s[46:47]
	s_and_saveexec_b64 s[8:9], s[18:19]
	v_lshl_add_u32 v0, v0, 3, s31
	v_add_u32_e32 v4, 0x181, v2
	ds_write_b64 v0, v[4:5]
	s_or_b64 exec, exec, s[8:9]
	s_bcnt1_i32_b64 s8, vcc
	s_bcnt1_i32_b64 s9, s[44:45]
	s_add_i32 s8, s28, s8
	s_add_i32 s28, s8, s9
	s_add_i32 s8, s30, 0x200
	s_cmp_gt_i32 s8, s10
	s_cbranch_scc1 .LBB0_1219

.LBB0_1255:
	s_add_i32 s8, s30, 0x380
	s_cmp_gt_i32 s8, s10
	s_cbranch_scc1 .Lsel1_single_4
	v_and_b32_e32 v7, 0xffff, v21
	v_and_b32_e32 v13, 0xffff, v22
	v_lshrrev_b32_e32 v5, 16, v21
	v_lshrrev_b32_e32 v11, 16, v22
	v_cmp_le_u32_e64 s[18:19], s29, v7
	v_cmp_le_u32_e64 s[8:9], s29, v5
	v_cmp_le_u32_e64 s[46:47], s29, v13
	v_cmp_le_u32_e64 s[58:59], s29, v11
	v_add_u32_e32 v6, 0x280, v2
	v_add_u32_e32 v12, 0x300, v2
	v_mbcnt_lo_u32_b32 v3, s18, 0
	v_mbcnt_hi_u32_b32 v3, s19, v3
	v_mbcnt_lo_u32_b32 v9, s46, 0
	v_mbcnt_hi_u32_b32 v9, s47, v9
	s_bcnt1_i32_b64 s98, s[18:19]
	s_bcnt1_i32_b64 s99, s[8:9]
	v_mbcnt_lo_u32_b32 v3, s8, v3
	v_mbcnt_hi_u32_b32 v3, s9, v3
	s_add_i32 s98, s98, s99
	s_bcnt1_i32_b64 s99, s[46:47]
	s_bcnt1_i32_b64 s96, s[58:59]
	v_mbcnt_lo_u32_b32 v9, s58, v9
	v_mbcnt_hi_u32_b32 v9, s59, v9
	s_add_i32 s99, s99, s96
	s_add_i32 s98, s28, s98
	v_add_u32_e32 v3, s28, v3
	s_add_i32 s99, s98, s99
	v_add_u32_e32 v9, s98, v9
	v_addc_co_u32_e64 v0, s[44:45], 0, v3, s[18:19]
	v_addc_co_u32_e64 v8, s[44:45], 0, v9, s[46:47]
	s_cmpk_gt_u32 s99, 0x2c0
	s_cbranch_scc1 .Lselslow_1_4
	s_and_saveexec_b64 s[44:45], s[18:19]
	v_lshl_add_u32 v14, v3, 3, s88
	ds_write_b64 v14, v[6:7]
	s_or_b64 exec, exec, s[44:45]
	s_and_saveexec_b64 s[44:45], s[8:9]
	v_lshl_add_u32 v14, v0, 3, s88
	v_add_u32_e32 v4, 0x281, v2
	ds_write_b64 v14, v[4:5]
	s_or_b64 exec, exec, s[44:45]
	s_and_saveexec_b64 s[44:45], s[46:47]
	v_lshl_add_u32 v14, v9, 3, s88
	ds_write_b64 v14, v[12:13]
	s_or_b64 exec, exec, s[44:45]
	s_and_saveexec_b64 s[44:45], s[58:59]
	v_lshl_add_u32 v14, v8, 3, s88
	v_add_u32_e32 v10, 0x301, v2
	ds_write_b64 v14, v[10:11]
	s_or_b64 exec, exec, s[44:45]
	s_mov_b32 s28, s99
	s_branch .Lselfin_1_4
.Lselslow_1_4:
	s_movk_i32 s96, 0x2c0
	v_cmp_gt_u32_e64 s[44:45], s96, v3
	v_cmp_gt_u32_e64 s[100:101], s96, v0
	v_cmp_gt_u32_e32 vcc, s96, v9
	s_and_b64 s[18:19], s[18:19], s[44:45]
	s_and_saveexec_b64 s[44:45], s[18:19]
	v_lshl_add_u32 v14, v3, 3, s88
	ds_write_b64 v14, v[6:7]
	s_or_b64 exec, exec, s[44:45]
	s_and_b64 s[8:9], s[8:9], s[100:101]
	v_cmp_gt_u32_e64 s[100:101], s96, v8
	s_and_saveexec_b64 s[44:45], s[8:9]
	v_lshl_add_u32 v14, v0, 3, s88
	v_add_u32_e32 v4, 0x281, v2
	ds_write_b64 v14, v[4:5]
	s_or_b64 exec, exec, s[44:45]
	s_and_b64 s[46:47], s[46:47], vcc
	s_and_saveexec_b64 s[44:45], s[46:47]
	v_lshl_add_u32 v14, v9, 3, s88
	ds_write_b64 v14, v[12:13]
	s_or_b64 exec, exec, s[44:45]
	s_and_b64 s[58:59], s[58:59], s[100:101]
	s_and_saveexec_b64 s[44:45], s[58:59]
	v_lshl_add_u32 v14, v8, 3, s88
	v_add_u32_e32 v10, 0x301, v2
	ds_write_b64 v14, v[10:11]
	s_or_b64 exec, exec, s[44:45]
	s_mov_b32 s28, s99
.Lselfin_1_4:
	s_branch .Lsel1_post_4
.Lsel1_single_4:
	v_and_b32_e32 v7, 0xffff, v21
	v_add_u32_e32 v6, 0x280, v2
	v_lshrrev_b32_e32 v5, 16, v21
	v_cmp_gt_u32_e64 s[44:45], s11, v6
	v_cmp_le_u32_e32 vcc, s29, v7
	v_cmp_le_u32_e64 s[46:47], s29, v5
	s_and_b64 s[18:19], s[44:45], vcc
	v_cndmask_b32_e64 v0, 0, 1, s[18:19]
	s_and_b64 s[8:9], s[44:45], s[46:47]
	v_cmp_ne_u32_e32 vcc, 0, v0
	v_cndmask_b32_e64 v3, 0, 1, s[8:9]
	v_cmp_ne_u32_e64 s[44:45], 0, v3
	v_mbcnt_lo_u32_b32 v3, vcc_lo, 0
	v_mbcnt_hi_u32_b32 v3, vcc_hi, v3
	v_mbcnt_lo_u32_b32 v3, s44, v3
	s_min_u32 s26, s28, 0x2c0
	v_mbcnt_hi_u32_b32 v3, s45, v3
	s_sub_i32 s33, 0x2c0, s26
	s_lshl_b32 s27, s26, 3
	v_cmp_gt_u32_e64 s[46:47], s33, v3
	s_add_i32 s31, s88, s27
	s_and_b64 s[18:19], s[18:19], s[46:47]
	s_and_saveexec_b64 s[26:27], s[18:19]
	v_lshl_add_u32 v4, v3, 3, s31
	ds_write_b64 v4, v[6:7]
	s_or_b64 exec, exec, s[26:27]
	v_add_u32_e32 v0, v3, v0
	v_cmp_gt_u32_e64 s[46:47], s33, v0
	s_and_b64 s[18:19], s[8:9], s[46:47]
	s_and_saveexec_b64 s[8:9], s[18:19]
	v_lshl_add_u32 v0, v0, 3, s31
	v_add_u32_e32 v4, 0x281, v2
	ds_write_b64 v0, v[4:5]
	s_or_b64 exec, exec, s[8:9]
	s_bcnt1_i32_b64 s8, vcc
	s_bcnt1_i32_b64 s9, s[44:45]
	s_add_i32 s8, s28, s8
	s_add_i32 s28, s8, s9
	s_add_i32 s8, s30, 0x300
	s_cmp_gt_i32 s8, s10
	s_cbranch_scc1 .LBB0_1221

.LBB0_1265:
	s_add_i32 s8, s30, 0x480
	s_cmp_gt_i32 s8, s10
	s_cbranch_scc1 .Lsel1_single_6
	v_and_b32_e32 v7, 0xffff, v23
	v_and_b32_e32 v13, 0xffff, v24
	v_lshrrev_b32_e32 v5, 16, v23
	v_lshrrev_b32_e32 v11, 16, v24
	v_cmp_le_u32_e64 s[18:19], s29, v7
	v_cmp_le_u32_e64 s[8:9], s29, v5
	v_cmp_le_u32_e64 s[46:47], s29, v13
	v_cmp_le_u32_e64 s[58:59], s29, v11
	v_add_u32_e32 v6, 0x380, v2
	v_add_u32_e32 v12, 0x400, v2
	v_mbcnt_lo_u32_b32 v3, s18, 0
	v_mbcnt_hi_u32_b32 v3, s19, v3
	v_mbcnt_lo_u32_b32 v9, s46, 0
	v_mbcnt_hi_u32_b32 v9, s47, v9
	s_bcnt1_i32_b64 s98, s[18:19]
	s_bcnt1_i32_b64 s99, s[8:9]
	v_mbcnt_lo_u32_b32 v3, s8, v3
	v_mbcnt_hi_u32_b32 v3, s9, v3
	s_add_i32 s98, s98, s99
	s_bcnt1_i32_b64 s99, s[46:47]
	s_bcnt1_i32_b64 s96, s[58:59]
	v_mbcnt_lo_u32_b32 v9, s58, v9
	v_mbcnt_hi_u32_b32 v9, s59, v9
	s_add_i32 s99, s99, s96
	s_add_i32 s98, s28, s98
	v_add_u32_e32 v3, s28, v3
	s_add_i32 s99, s98, s99
	v_add_u32_e32 v9, s98, v9
	v_addc_co_u32_e64 v0, s[44:45], 0, v3, s[18:19]
	v_addc_co_u32_e64 v8, s[44:45], 0, v9, s[46:47]
	s_cmpk_gt_u32 s99, 0x2c0
	s_cbranch_scc1 .Lselslow_1_6
	s_and_saveexec_b64 s[44:45], s[18:19]
	v_lshl_add_u32 v14, v3, 3, s88
	ds_write_b64 v14, v[6:7]
	s_or_b64 exec, exec, s[44:45]
	s_and_saveexec_b64 s[44:45], s[8:9]
	v_lshl_add_u32 v14, v0, 3, s88
	v_add_u32_e32 v4, 0x381, v2
	ds_write_b64 v14, v[4:5]
	s_or_b64 exec, exec, s[44:45]
	s_and_saveexec_b64 s[44:45], s[46:47]
	v_lshl_add_u32 v14, v9, 3, s88
	ds_write_b64 v14, v[12:13]
	s_or_b64 exec, exec, s[44:45]
	s_and_saveexec_b64 s[44:45], s[58:59]
	v_lshl_add_u32 v14, v8, 3, s88
	v_add_u32_e32 v10, 0x401, v2
	ds_write_b64 v14, v[10:11]
	s_or_b64 exec, exec, s[44:45]
	s_mov_b32 s28, s99
	s_branch .Lselfin_1_6
.Lselslow_1_6:
	s_movk_i32 s96, 0x2c0
	v_cmp_gt_u32_e64 s[44:45], s96, v3
	v_cmp_gt_u32_e64 s[100:101], s96, v0
	v_cmp_gt_u32_e32 vcc, s96, v9
	s_and_b64 s[18:19], s[18:19], s[44:45]
	s_and_saveexec_b64 s[44:45], s[18:19]
	v_lshl_add_u32 v14, v3, 3, s88
	ds_write_b64 v14, v[6:7]
	s_or_b64 exec, exec, s[44:45]
	s_and_b64 s[8:9], s[8:9], s[100:101]
	v_cmp_gt_u32_e64 s[100:101], s96, v8
	s_and_saveexec_b64 s[44:45], s[8:9]
	v_lshl_add_u32 v14, v0, 3, s88
	v_add_u32_e32 v4, 0x381, v2
	ds_write_b64 v14, v[4:5]
	s_or_b64 exec, exec, s[44:45]
	s_and_b64 s[46:47], s[46:47], vcc
	s_and_saveexec_b64 s[44:45], s[46:47]
	v_lshl_add_u32 v14, v9, 3, s88
	ds_write_b64 v14, v[12:13]
	s_or_b64 exec, exec, s[44:45]
	s_and_b64 s[58:59], s[58:59], s[100:101]
	s_and_saveexec_b64 s[44:45], s[58:59]
	v_lshl_add_u32 v14, v8, 3, s88
	v_add_u32_e32 v10, 0x401, v2
	ds_write_b64 v14, v[10:11]
	s_or_b64 exec, exec, s[44:45]
	s_mov_b32 s28, s99
.Lselfin_1_6:
	s_branch .Lsel1_post_6
.Lsel1_single_6:
	v_and_b32_e32 v7, 0xffff, v23
	v_add_u32_e32 v6, 0x380, v2
	v_lshrrev_b32_e32 v5, 16, v23
	v_cmp_gt_u32_e64 s[44:45], s11, v6
	v_cmp_le_u32_e32 vcc, s29, v7
	v_cmp_le_u32_e64 s[46:47], s29, v5
	s_and_b64 s[18:19], s[44:45], vcc
	v_cndmask_b32_e64 v0, 0, 1, s[18:19]
	s_and_b64 s[8:9], s[44:45], s[46:47]
	v_cmp_ne_u32_e32 vcc, 0, v0
	v_cndmask_b32_e64 v3, 0, 1, s[8:9]
	v_cmp_ne_u32_e64 s[44:45], 0, v3
	v_mbcnt_lo_u32_b32 v3, vcc_lo, 0
	v_mbcnt_hi_u32_b32 v3, vcc_hi, v3
	v_mbcnt_lo_u32_b32 v3, s44, v3
	s_min_u32 s26, s28, 0x2c0
	v_mbcnt_hi_u32_b32 v3, s45, v3
	s_sub_i32 s33, 0x2c0, s26
	s_lshl_b32 s27, s26, 3
	v_cmp_gt_u32_e64 s[46:47], s33, v3
	s_add_i32 s31, s88, s27
	s_and_b64 s[18:19], s[18:19], s[46:47]
	s_and_saveexec_b64 s[26:27], s[18:19]
	v_lshl_add_u32 v4, v3, 3, s31
	ds_write_b64 v4, v[6:7]
	s_or_b64 exec, exec, s[26:27]
	v_add_u32_e32 v0, v3, v0
	v_cmp_gt_u32_e64 s[46:47], s33, v0
	s_and_b64 s[18:19], s[8:9], s[46:47]
	s_and_saveexec_b64 s[8:9], s[18:19]
	v_lshl_add_u32 v0, v0, 3, s31
	v_add_u32_e32 v4, 0x381, v2
	ds_write_b64 v0, v[4:5]
	s_or_b64 exec, exec, s[8:9]
	s_bcnt1_i32_b64 s8, vcc
	s_bcnt1_i32_b64 s9, s[44:45]
	s_add_i32 s8, s28, s8
	s_add_i32 s28, s8, s9
	s_add_i32 s8, s30, 0x400
	s_cmp_gt_i32 s8, s10
	s_cbranch_scc1 .LBB0_1223

.LBB0_1275:
	s_add_i32 s8, s30, 0x580
	s_cmp_gt_i32 s8, s10
	s_cbranch_scc1 .Lsel1_single_8
	v_and_b32_e32 v7, 0xffff, v25
	v_and_b32_e32 v13, 0xffff, v26
	v_lshrrev_b32_e32 v5, 16, v25
	v_lshrrev_b32_e32 v11, 16, v26
	v_cmp_le_u32_e64 s[18:19], s29, v7
	v_cmp_le_u32_e64 s[8:9], s29, v5
	v_cmp_le_u32_e64 s[46:47], s29, v13
	v_cmp_le_u32_e64 s[58:59], s29, v11
	v_add_u32_e32 v6, 0x480, v2
	v_add_u32_e32 v12, 0x500, v2
	v_mbcnt_lo_u32_b32 v3, s18, 0
	v_mbcnt_hi_u32_b32 v3, s19, v3
	v_mbcnt_lo_u32_b32 v9, s46, 0
	v_mbcnt_hi_u32_b32 v9, s47, v9
	s_bcnt1_i32_b64 s98, s[18:19]
	s_bcnt1_i32_b64 s99, s[8:9]
	v_mbcnt_lo_u32_b32 v3, s8, v3
	v_mbcnt_hi_u32_b32 v3, s9, v3
	s_add_i32 s98, s98, s99
	s_bcnt1_i32_b64 s99, s[46:47]
	s_bcnt1_i32_b64 s96, s[58:59]
	v_mbcnt_lo_u32_b32 v9, s58, v9
	v_mbcnt_hi_u32_b32 v9, s59, v9
	s_add_i32 s99, s99, s96
	s_add_i32 s98, s28, s98
	v_add_u32_e32 v3, s28, v3
	s_add_i32 s99, s98, s99
	v_add_u32_e32 v9, s98, v9
	v_addc_co_u32_e64 v0, s[44:45], 0, v3, s[18:19]
	v_addc_co_u32_e64 v8, s[44:45], 0, v9, s[46:47]
	s_cmpk_gt_u32 s99, 0x2c0
	s_cbranch_scc1 .Lselslow_1_8
	s_and_saveexec_b64 s[44:45], s[18:19]
	v_lshl_add_u32 v14, v3, 3, s88
	ds_write_b64 v14, v[6:7]
	s_or_b64 exec, exec, s[44:45]
	s_and_saveexec_b64 s[44:45], s[8:9]
	v_lshl_add_u32 v14, v0, 3, s88
	v_add_u32_e32 v4, 0x481, v2
	ds_write_b64 v14, v[4:5]
	s_or_b64 exec, exec, s[44:45]
	s_and_saveexec_b64 s[44:45], s[46:47]
	v_lshl_add_u32 v14, v9, 3, s88
	ds_write_b64 v14, v[12:13]
	s_or_b64 exec, exec, s[44:45]
	s_and_saveexec_b64 s[44:45], s[58:59]
	v_lshl_add_u32 v14, v8, 3, s88
	v_add_u32_e32 v10, 0x501, v2
	ds_write_b64 v14, v[10:11]
	s_or_b64 exec, exec, s[44:45]
	s_mov_b32 s28, s99
	s_branch .Lselfin_1_8
.Lselslow_1_8:
	s_movk_i32 s96, 0x2c0
	v_cmp_gt_u32_e64 s[44:45], s96, v3
	v_cmp_gt_u32_e64 s[100:101], s96, v0
	v_cmp_gt_u32_e32 vcc, s96, v9
	s_and_b64 s[18:19], s[18:19], s[44:45]
	s_and_saveexec_b64 s[44:45], s[18:19]
	v_lshl_add_u32 v14, v3, 3, s88
	ds_write_b64 v14, v[6:7]
	s_or_b64 exec, exec, s[44:45]
	s_and_b64 s[8:9], s[8:9], s[100:101]
	v_cmp_gt_u32_e64 s[100:101], s96, v8
	s_and_saveexec_b64 s[44:45], s[8:9]
	v_lshl_add_u32 v14, v0, 3, s88
	v_add_u32_e32 v4, 0x481, v2
	ds_write_b64 v14, v[4:5]
	s_or_b64 exec, exec, s[44:45]
	s_and_b64 s[46:47], s[46:47], vcc
	s_and_saveexec_b64 s[44:45], s[46:47]
	v_lshl_add_u32 v14, v9, 3, s88
	ds_write_b64 v14, v[12:13]
	s_or_b64 exec, exec, s[44:45]
	s_and_b64 s[58:59], s[58:59], s[100:101]
	s_and_saveexec_b64 s[44:45], s[58:59]
	v_lshl_add_u32 v14, v8, 3, s88
	v_add_u32_e32 v10, 0x501, v2
	ds_write_b64 v14, v[10:11]
	s_or_b64 exec, exec, s[44:45]
	s_mov_b32 s28, s99
.Lselfin_1_8:
	s_branch .Lsel1_post_8
.Lsel1_single_8:
	v_and_b32_e32 v7, 0xffff, v25
	v_add_u32_e32 v6, 0x480, v2
	v_lshrrev_b32_e32 v5, 16, v25
	v_cmp_gt_u32_e64 s[44:45], s11, v6
	v_cmp_le_u32_e32 vcc, s29, v7
	v_cmp_le_u32_e64 s[46:47], s29, v5
	s_and_b64 s[18:19], s[44:45], vcc
	v_cndmask_b32_e64 v0, 0, 1, s[18:19]
	s_and_b64 s[8:9], s[44:45], s[46:47]
	v_cmp_ne_u32_e32 vcc, 0, v0
	v_cndmask_b32_e64 v3, 0, 1, s[8:9]
	v_cmp_ne_u32_e64 s[44:45], 0, v3
	v_mbcnt_lo_u32_b32 v3, vcc_lo, 0
	v_mbcnt_hi_u32_b32 v3, vcc_hi, v3
	v_mbcnt_lo_u32_b32 v3, s44, v3
	s_min_u32 s26, s28, 0x2c0
	v_mbcnt_hi_u32_b32 v3, s45, v3
	s_sub_i32 s33, 0x2c0, s26
	s_lshl_b32 s27, s26, 3
	v_cmp_gt_u32_e64 s[46:47], s33, v3
	s_add_i32 s31, s88, s27
	s_and_b64 s[18:19], s[18:19], s[46:47]
	s_and_saveexec_b64 s[26:27], s[18:19]
	v_lshl_add_u32 v4, v3, 3, s31
	ds_write_b64 v4, v[6:7]
	s_or_b64 exec, exec, s[26:27]
	v_add_u32_e32 v0, v3, v0
	v_cmp_gt_u32_e64 s[46:47], s33, v0
	s_and_b64 s[18:19], s[8:9], s[46:47]
	s_and_saveexec_b64 s[8:9], s[18:19]
	v_lshl_add_u32 v0, v0, 3, s31
	v_add_u32_e32 v4, 0x481, v2
	ds_write_b64 v0, v[4:5]
	s_or_b64 exec, exec, s[8:9]
	s_bcnt1_i32_b64 s8, vcc
	s_bcnt1_i32_b64 s9, s[44:45]
	s_add_i32 s8, s28, s8
	s_add_i32 s28, s8, s9
	s_add_i32 s8, s30, 0x500
	s_cmp_gt_i32 s8, s10
	s_cbranch_scc1 .LBB0_1225

.LBB0_1285:
	s_add_i32 s8, s30, 0x680
	s_cmp_gt_i32 s8, s10
	s_cbranch_scc1 .Lsel1_single_10
	v_and_b32_e32 v7, 0xffff, v27
	v_and_b32_e32 v13, 0xffff, v28
	v_lshrrev_b32_e32 v5, 16, v27
	v_lshrrev_b32_e32 v11, 16, v28
	v_cmp_le_u32_e64 s[18:19], s29, v7
	v_cmp_le_u32_e64 s[8:9], s29, v5
	v_cmp_le_u32_e64 s[46:47], s29, v13
	v_cmp_le_u32_e64 s[58:59], s29, v11
	v_add_u32_e32 v6, 0x580, v2
	v_add_u32_e32 v12, 0x600, v2
	v_mbcnt_lo_u32_b32 v3, s18, 0
	v_mbcnt_hi_u32_b32 v3, s19, v3
	v_mbcnt_lo_u32_b32 v9, s46, 0
	v_mbcnt_hi_u32_b32 v9, s47, v9
	s_bcnt1_i32_b64 s98, s[18:19]
	s_bcnt1_i32_b64 s99, s[8:9]
	v_mbcnt_lo_u32_b32 v3, s8, v3
	v_mbcnt_hi_u32_b32 v3, s9, v3
	s_add_i32 s98, s98, s99
	s_bcnt1_i32_b64 s99, s[46:47]
	s_bcnt1_i32_b64 s96, s[58:59]
	v_mbcnt_lo_u32_b32 v9, s58, v9
	v_mbcnt_hi_u32_b32 v9, s59, v9
	s_add_i32 s99, s99, s96
	s_add_i32 s98, s28, s98
	v_add_u32_e32 v3, s28, v3
	s_add_i32 s99, s98, s99
	v_add_u32_e32 v9, s98, v9
	v_addc_co_u32_e64 v0, s[44:45], 0, v3, s[18:19]
	v_addc_co_u32_e64 v8, s[44:45], 0, v9, s[46:47]
	s_cmpk_gt_u32 s99, 0x2c0
	s_cbranch_scc1 .Lselslow_1_10
	s_and_saveexec_b64 s[44:45], s[18:19]
	v_lshl_add_u32 v14, v3, 3, s88
	ds_write_b64 v14, v[6:7]
	s_or_b64 exec, exec, s[44:45]
	s_and_saveexec_b64 s[44:45], s[8:9]
	v_lshl_add_u32 v14, v0, 3, s88
	v_add_u32_e32 v4, 0x581, v2
	ds_write_b64 v14, v[4:5]
	s_or_b64 exec, exec, s[44:45]
	s_and_saveexec_b64 s[44:45], s[46:47]
	v_lshl_add_u32 v14, v9, 3, s88
	ds_write_b64 v14, v[12:13]
	s_or_b64 exec, exec, s[44:45]
	s_and_saveexec_b64 s[44:45], s[58:59]
	v_lshl_add_u32 v14, v8, 3, s88
	v_add_u32_e32 v10, 0x601, v2
	ds_write_b64 v14, v[10:11]
	s_or_b64 exec, exec, s[44:45]
	s_mov_b32 s28, s99
	s_branch .Lselfin_1_10
.Lselslow_1_10:
	s_movk_i32 s96, 0x2c0
	v_cmp_gt_u32_e64 s[44:45], s96, v3
	v_cmp_gt_u32_e64 s[100:101], s96, v0
	v_cmp_gt_u32_e32 vcc, s96, v9
	s_and_b64 s[18:19], s[18:19], s[44:45]
	s_and_saveexec_b64 s[44:45], s[18:19]
	v_lshl_add_u32 v14, v3, 3, s88
	ds_write_b64 v14, v[6:7]
	s_or_b64 exec, exec, s[44:45]
	s_and_b64 s[8:9], s[8:9], s[100:101]
	v_cmp_gt_u32_e64 s[100:101], s96, v8
	s_and_saveexec_b64 s[44:45], s[8:9]
	v_lshl_add_u32 v14, v0, 3, s88
	v_add_u32_e32 v4, 0x581, v2
	ds_write_b64 v14, v[4:5]
	s_or_b64 exec, exec, s[44:45]
	s_and_b64 s[46:47], s[46:47], vcc
	s_and_saveexec_b64 s[44:45], s[46:47]
	v_lshl_add_u32 v14, v9, 3, s88
	ds_write_b64 v14, v[12:13]
	s_or_b64 exec, exec, s[44:45]
	s_and_b64 s[58:59], s[58:59], s[100:101]
	s_and_saveexec_b64 s[44:45], s[58:59]
	v_lshl_add_u32 v14, v8, 3, s88
	v_add_u32_e32 v10, 0x601, v2
	ds_write_b64 v14, v[10:11]
	s_or_b64 exec, exec, s[44:45]
	s_mov_b32 s28, s99
.Lselfin_1_10:
	s_branch .Lsel1_post_10
.Lsel1_single_10:
	v_and_b32_e32 v7, 0xffff, v27
	v_add_u32_e32 v6, 0x580, v2
	v_lshrrev_b32_e32 v5, 16, v27
	v_cmp_gt_u32_e64 s[44:45], s11, v6
	v_cmp_le_u32_e32 vcc, s29, v7
	v_cmp_le_u32_e64 s[46:47], s29, v5
	s_and_b64 s[18:19], s[44:45], vcc
	v_cndmask_b32_e64 v0, 0, 1, s[18:19]
	s_and_b64 s[8:9], s[44:45], s[46:47]
	v_cmp_ne_u32_e32 vcc, 0, v0
	v_cndmask_b32_e64 v3, 0, 1, s[8:9]
	v_cmp_ne_u32_e64 s[44:45], 0, v3
	v_mbcnt_lo_u32_b32 v3, vcc_lo, 0
	v_mbcnt_hi_u32_b32 v3, vcc_hi, v3
	v_mbcnt_lo_u32_b32 v3, s44, v3
	s_min_u32 s26, s28, 0x2c0
	v_mbcnt_hi_u32_b32 v3, s45, v3
	s_sub_i32 s33, 0x2c0, s26
	s_lshl_b32 s27, s26, 3
	v_cmp_gt_u32_e64 s[46:47], s33, v3
	s_add_i32 s31, s88, s27
	s_and_b64 s[18:19], s[18:19], s[46:47]
	s_and_saveexec_b64 s[26:27], s[18:19]
	v_lshl_add_u32 v4, v3, 3, s31
	ds_write_b64 v4, v[6:7]
	s_or_b64 exec, exec, s[26:27]
	v_add_u32_e32 v0, v3, v0
	v_cmp_gt_u32_e64 s[46:47], s33, v0
	s_and_b64 s[18:19], s[8:9], s[46:47]
	s_and_saveexec_b64 s[8:9], s[18:19]
	v_lshl_add_u32 v0, v0, 3, s31
	v_add_u32_e32 v4, 0x581, v2
	ds_write_b64 v0, v[4:5]
	s_or_b64 exec, exec, s[8:9]
	s_bcnt1_i32_b64 s8, vcc
	s_bcnt1_i32_b64 s9, s[44:45]
	s_add_i32 s8, s28, s8
	s_add_i32 s28, s8, s9
	s_add_i32 s8, s30, 0x600
	s_cmp_gt_i32 s8, s10
	s_cbranch_scc1 .LBB0_1227

.LBB0_1295:
	s_add_i32 s8, s30, 0x780
	s_cmp_gt_i32 s8, s10
	s_cbranch_scc1 .Lsel1_single_12
	v_and_b32_e32 v7, 0xffff, v29
	v_and_b32_e32 v13, 0xffff, v30
	v_lshrrev_b32_e32 v5, 16, v29
	v_lshrrev_b32_e32 v11, 16, v30
	v_cmp_le_u32_e64 s[18:19], s29, v7
	v_cmp_le_u32_e64 s[8:9], s29, v5
	v_cmp_le_u32_e64 s[46:47], s29, v13
	v_cmp_le_u32_e64 s[58:59], s29, v11
	v_add_u32_e32 v6, 0x680, v2
	v_add_u32_e32 v12, 0x700, v2
	v_mbcnt_lo_u32_b32 v3, s18, 0
	v_mbcnt_hi_u32_b32 v3, s19, v3
	v_mbcnt_lo_u32_b32 v9, s46, 0
	v_mbcnt_hi_u32_b32 v9, s47, v9
	s_bcnt1_i32_b64 s98, s[18:19]
	s_bcnt1_i32_b64 s99, s[8:9]
	v_mbcnt_lo_u32_b32 v3, s8, v3
	v_mbcnt_hi_u32_b32 v3, s9, v3
	s_add_i32 s98, s98, s99
	s_bcnt1_i32_b64 s99, s[46:47]
	s_bcnt1_i32_b64 s96, s[58:59]
	v_mbcnt_lo_u32_b32 v9, s58, v9
	v_mbcnt_hi_u32_b32 v9, s59, v9
	s_add_i32 s99, s99, s96
	s_add_i32 s98, s28, s98
	v_add_u32_e32 v3, s28, v3
	s_add_i32 s99, s98, s99
	v_add_u32_e32 v9, s98, v9
	v_addc_co_u32_e64 v0, s[44:45], 0, v3, s[18:19]
	v_addc_co_u32_e64 v8, s[44:45], 0, v9, s[46:47]
	s_cmpk_gt_u32 s99, 0x2c0
	s_cbranch_scc1 .Lselslow_1_12
	s_and_saveexec_b64 s[44:45], s[18:19]
	v_lshl_add_u32 v14, v3, 3, s88
	ds_write_b64 v14, v[6:7]
	s_or_b64 exec, exec, s[44:45]
	s_and_saveexec_b64 s[44:45], s[8:9]
	v_lshl_add_u32 v14, v0, 3, s88
	v_add_u32_e32 v4, 0x681, v2
	ds_write_b64 v14, v[4:5]
	s_or_b64 exec, exec, s[44:45]
	s_and_saveexec_b64 s[44:45], s[46:47]
	v_lshl_add_u32 v14, v9, 3, s88
	ds_write_b64 v14, v[12:13]
	s_or_b64 exec, exec, s[44:45]
	s_and_saveexec_b64 s[44:45], s[58:59]
	v_lshl_add_u32 v14, v8, 3, s88
	v_add_u32_e32 v10, 0x701, v2
	ds_write_b64 v14, v[10:11]
	s_or_b64 exec, exec, s[44:45]
	s_mov_b32 s28, s99
	s_branch .Lselfin_1_12
.Lselslow_1_12:
	s_movk_i32 s96, 0x2c0
	v_cmp_gt_u32_e64 s[44:45], s96, v3
	v_cmp_gt_u32_e64 s[100:101], s96, v0
	v_cmp_gt_u32_e32 vcc, s96, v9
	s_and_b64 s[18:19], s[18:19], s[44:45]
	s_and_saveexec_b64 s[44:45], s[18:19]
	v_lshl_add_u32 v14, v3, 3, s88
	ds_write_b64 v14, v[6:7]
	s_or_b64 exec, exec, s[44:45]
	s_and_b64 s[8:9], s[8:9], s[100:101]
	v_cmp_gt_u32_e64 s[100:101], s96, v8
	s_and_saveexec_b64 s[44:45], s[8:9]
	v_lshl_add_u32 v14, v0, 3, s88
	v_add_u32_e32 v4, 0x681, v2
	ds_write_b64 v14, v[4:5]
	s_or_b64 exec, exec, s[44:45]
	s_and_b64 s[46:47], s[46:47], vcc
	s_and_saveexec_b64 s[44:45], s[46:47]
	v_lshl_add_u32 v14, v9, 3, s88
	ds_write_b64 v14, v[12:13]
	s_or_b64 exec, exec, s[44:45]
	s_and_b64 s[58:59], s[58:59], s[100:101]
	s_and_saveexec_b64 s[44:45], s[58:59]
	v_lshl_add_u32 v14, v8, 3, s88
	v_add_u32_e32 v10, 0x701, v2
	ds_write_b64 v14, v[10:11]
	s_or_b64 exec, exec, s[44:45]
	s_mov_b32 s28, s99
.Lselfin_1_12:
	s_branch .Lsel1_post_12
.Lsel1_single_12:
	v_and_b32_e32 v7, 0xffff, v29
	v_add_u32_e32 v6, 0x680, v2
	v_lshrrev_b32_e32 v5, 16, v29
	v_cmp_gt_u32_e64 s[44:45], s11, v6
	v_cmp_le_u32_e32 vcc, s29, v7
	v_cmp_le_u32_e64 s[46:47], s29, v5
	s_and_b64 s[18:19], s[44:45], vcc
	v_cndmask_b32_e64 v0, 0, 1, s[18:19]
	s_and_b64 s[8:9], s[44:45], s[46:47]
	v_cmp_ne_u32_e32 vcc, 0, v0
	v_cndmask_b32_e64 v3, 0, 1, s[8:9]
	v_cmp_ne_u32_e64 s[44:45], 0, v3
	v_mbcnt_lo_u32_b32 v3, vcc_lo, 0
	v_mbcnt_hi_u32_b32 v3, vcc_hi, v3
	v_mbcnt_lo_u32_b32 v3, s44, v3
	s_min_u32 s26, s28, 0x2c0
	v_mbcnt_hi_u32_b32 v3, s45, v3
	s_sub_i32 s33, 0x2c0, s26
	s_lshl_b32 s27, s26, 3
	v_cmp_gt_u32_e64 s[46:47], s33, v3
	s_add_i32 s31, s88, s27
	s_and_b64 s[18:19], s[18:19], s[46:47]
	s_and_saveexec_b64 s[26:27], s[18:19]
	v_lshl_add_u32 v4, v3, 3, s31
	ds_write_b64 v4, v[6:7]
	s_or_b64 exec, exec, s[26:27]
	v_add_u32_e32 v0, v3, v0
	v_cmp_gt_u32_e64 s[46:47], s33, v0
	s_and_b64 s[18:19], s[8:9], s[46:47]
	s_and_saveexec_b64 s[8:9], s[18:19]
	v_lshl_add_u32 v0, v0, 3, s31
	v_add_u32_e32 v4, 0x681, v2
	ds_write_b64 v0, v[4:5]
	s_or_b64 exec, exec, s[8:9]
	s_bcnt1_i32_b64 s8, vcc
	s_bcnt1_i32_b64 s9, s[44:45]
	s_add_i32 s8, s28, s8
	s_add_i32 s28, s8, s9
	s_add_i32 s8, s30, 0x700
	s_cmp_gt_i32 s8, s10
	s_cbranch_scc1 .LBB0_1229
